# s11 + PROJ: a workgroup's last unit stores its tile write-through (sc1) so the ARRIVE's release write-back finds few dirty lines
# speedup vs baseline: 1.0121x; 1.0063x over previous
; __device__ __forceinline__ unsigned cvt_pk_f16(float lo, float hi) { f32x2 v = {lo, hi}; h16x2 b = __builtin_convertvector(v, h16x2); return __builtin_bit_cast(unsigned, b); }
;     __device__ __forceinline__ void operator()(const f32x4 (&acc)[2][2][4][2], const Unit& u, int wr, int wc, int fr, int fq) const {
;         const int row0 = u.pm * BM + wr * 64 + fr, col0 = u.pn * BM + wc * 32 + 8 * fq;
; #pragma unroll
;         for (int ai = 0; ai < 2; ++ai)
; #pragma unroll
;             for (int m = 0; m < 4; ++m) { h16* rowp = C + (size_t)(row0 + ai * HALF + m * 16) * ldc + col0;
; #pragma unroll
;                 for (int bj = 0; bj < 2; ++bj) { const f32x4 v0 = acc[ai][bj][m][0], v1 = acc[ai][bj][m][1];
;                     u32x4 w; w.x = cvt_pk_f16(v0[0], v0[1]); w.y = cvt_pk_f16(v0[2], v0[3]); w.z = cvt_pk_f16(v1[0], v1[1]); w.w = cvt_pk_f16(v1[2], v1[3]);
;                     *(u32x4*)(rowp + bj * HALF) = w; } }
.LBB0_983:
	s_and_b64 vcc, exec, s[38:39]
	s_cbranch_vccz .Lproj_epi_last
	v_and_b32_e32 v224, -9, v140
	v_and_b32_e32 v225, 8, v140
	v_and_b32_e32 v226, 0x60, v142
	v_lshlrev_b32_e32 v225, 2, v225
	v_add3_u32 v226, v142, v226, v225
	v_lshl_add_u32 v150, s35, 8, v224
	v_lshl_or_b32 v144, s34, 8, v226
	v_ashrrev_i32_e32 v145, 31, v144
	v_mov_b64_e32 v[146:147], s[16:17]
	v_lshlrev_b64 v[144:145], 1, v[144:145]
	s_mov_b64 s[52:53], 0x1c000
	v_mad_i64_i32 v[152:153], s[34:35], v150, s91, v[146:147]
	v_lshl_add_u64 v[152:153], v[152:153], 0, v[144:145]
	v_add_u32_e32 v151, 0x10, v150
	v_mad_i64_i32 v[154:155], s[34:35], v151, s91, v[146:147]
	v_lshl_add_u64 v[154:155], v[154:155], 0, v[144:145]
	v_add_u32_e32 v151, 0x20, v150
	v_mad_i64_i32 v[156:157], s[34:35], v151, s91, v[146:147]
	v_lshl_add_u64 v[156:157], v[156:157], 0, v[144:145]
	v_add_u32_e32 v151, 0x30, v150
	v_mad_i64_i32 v[158:159], s[34:35], v151, s91, v[146:147]
	v_lshl_add_u64 v[158:159], v[158:159], 0, v[144:145]
	v_add_u32_e32 v151, 0x80, v150
	v_mad_i64_i32 v[160:161], s[34:35], v151, s91, v[146:147]
	v_lshl_add_u64 v[160:161], v[160:161], 0, v[144:145]
	v_add_u32_e32 v151, 0x90, v150
	v_mad_i64_i32 v[162:163], s[34:35], v151, s91, v[146:147]
	v_lshl_add_u64 v[162:163], v[162:163], 0, v[144:145]
	v_add_u32_e32 v151, 0xa0, v150
	v_mad_i64_i32 v[164:165], s[34:35], v151, s91, v[146:147]
	v_lshl_add_u64 v[164:165], v[164:165], 0, v[144:145]
	v_add_u32_e32 v151, 0xb0, v150
	v_mad_i64_i32 v[166:167], s[34:35], v151, s91, v[146:147]
	v_lshl_add_u64 v[166:167], v[166:167], 0, v[144:145]
	v_cvt_pk_f16_f32 v126, v126, v127
	v_cvt_pk_f16_f32 v127, v128, v129
	v_cvt_pk_f16_f32 v128, v122, v123
	v_cvt_pk_f16_f32 v129, v124, v125
	v_cvt_pk_f16_f32 v110, v110, v111
	v_cvt_pk_f16_f32 v111, v112, v113
	v_cvt_pk_f16_f32 v112, v106, v107
	v_cvt_pk_f16_f32 v113, v108, v109
	v_mov_b32_e32 v218, v110
	v_mov_b32_e32 v219, v111
	v_mov_b32_e32 v220, v112
	v_mov_b32_e32 v221, v113
	s_nop 1
	v_mov_b32_dpp v110, v126 row_ror:8 row_mask:0xf bank_mask:0x3
	v_mov_b32_dpp v111, v127 row_ror:8 row_mask:0xf bank_mask:0x3
	v_mov_b32_dpp v112, v128 row_ror:8 row_mask:0xf bank_mask:0x3
	v_mov_b32_dpp v113, v129 row_ror:8 row_mask:0xf bank_mask:0x3
	v_mov_b32_dpp v126, v218 row_ror:8 row_mask:0xf bank_mask:0xc
	v_mov_b32_dpp v127, v219 row_ror:8 row_mask:0xf bank_mask:0xc
	v_mov_b32_dpp v128, v220 row_ror:8 row_mask:0xf bank_mask:0xc
	v_mov_b32_dpp v129, v221 row_ror:8 row_mask:0xf bank_mask:0xc
	v_lshl_add_u64 v[168:169], v[152:153], 0, s[52:53]
	global_store_dwordx4 v[152:153], v[126:129], off
	global_store_dwordx4 v[168:169], v[110:113], off
	v_cvt_pk_f16_f32 v118, v118, v119
	v_cvt_pk_f16_f32 v119, v120, v121
	v_cvt_pk_f16_f32 v120, v114, v115
	v_cvt_pk_f16_f32 v121, v116, v117
	v_cvt_pk_f16_f32 v92, v92, v93
	v_cvt_pk_f16_f32 v93, v94, v95
	v_cvt_pk_f16_f32 v94, v88, v89
	v_cvt_pk_f16_f32 v95, v90, v91
	v_mov_b32_e32 v218, v92
	v_mov_b32_e32 v219, v93
	v_mov_b32_e32 v220, v94
	v_mov_b32_e32 v221, v95
	s_nop 1
	v_mov_b32_dpp v92, v118 row_ror:8 row_mask:0xf bank_mask:0x3
	v_mov_b32_dpp v93, v119 row_ror:8 row_mask:0xf bank_mask:0x3
	v_mov_b32_dpp v94, v120 row_ror:8 row_mask:0xf bank_mask:0x3
	v_mov_b32_dpp v95, v121 row_ror:8 row_mask:0xf bank_mask:0x3
	v_mov_b32_dpp v118, v218 row_ror:8 row_mask:0xf bank_mask:0xc
	v_mov_b32_dpp v119, v219 row_ror:8 row_mask:0xf bank_mask:0xc
	v_mov_b32_dpp v120, v220 row_ror:8 row_mask:0xf bank_mask:0xc
	v_mov_b32_dpp v121, v221 row_ror:8 row_mask:0xf bank_mask:0xc
	v_lshl_add_u64 v[168:169], v[154:155], 0, s[52:53]
	global_store_dwordx4 v[154:155], v[118:121], off
	global_store_dwordx4 v[168:169], v[92:95], off
	v_cvt_pk_f16_f32 v102, v102, v103
	v_cvt_pk_f16_f32 v103, v104, v105
	v_cvt_pk_f16_f32 v104, v98, v99
	v_cvt_pk_f16_f32 v105, v100, v101
	v_cvt_pk_f16_f32 v76, v76, v77
	v_cvt_pk_f16_f32 v77, v78, v79
	v_cvt_pk_f16_f32 v78, v72, v73
	v_cvt_pk_f16_f32 v79, v74, v75
	v_mov_b32_e32 v218, v76
	v_mov_b32_e32 v219, v77
	v_mov_b32_e32 v220, v78
	v_mov_b32_e32 v221, v79
	s_nop 1
	v_mov_b32_dpp v76, v102 row_ror:8 row_mask:0xf bank_mask:0x3
	v_mov_b32_dpp v77, v103 row_ror:8 row_mask:0xf bank_mask:0x3
	v_mov_b32_dpp v78, v104 row_ror:8 row_mask:0xf bank_mask:0x3
	v_mov_b32_dpp v79, v105 row_ror:8 row_mask:0xf bank_mask:0x3
	v_mov_b32_dpp v102, v218 row_ror:8 row_mask:0xf bank_mask:0xc
	v_mov_b32_dpp v103, v219 row_ror:8 row_mask:0xf bank_mask:0xc
	v_mov_b32_dpp v104, v220 row_ror:8 row_mask:0xf bank_mask:0xc
	v_mov_b32_dpp v105, v221 row_ror:8 row_mask:0xf bank_mask:0xc
	v_lshl_add_u64 v[168:169], v[156:157], 0, s[52:53]
	global_store_dwordx4 v[156:157], v[102:105], off
	global_store_dwordx4 v[168:169], v[76:79], off
	v_cvt_pk_f16_f32 v84, v84, v85
	v_cvt_pk_f16_f32 v85, v86, v87
	v_cvt_pk_f16_f32 v86, v80, v81
	v_cvt_pk_f16_f32 v87, v82, v83
	v_cvt_pk_f16_f32 v68, v68, v69
	v_cvt_pk_f16_f32 v69, v70, v71
	v_cvt_pk_f16_f32 v70, v64, v65
	v_cvt_pk_f16_f32 v71, v66, v67
	v_mov_b32_e32 v218, v68
	v_mov_b32_e32 v219, v69
	v_mov_b32_e32 v220, v70
	v_mov_b32_e32 v221, v71
	s_nop 1
	v_mov_b32_dpp v68, v84 row_ror:8 row_mask:0xf bank_mask:0x3
	v_mov_b32_dpp v69, v85 row_ror:8 row_mask:0xf bank_mask:0x3
	v_mov_b32_dpp v70, v86 row_ror:8 row_mask:0xf bank_mask:0x3
	v_mov_b32_dpp v71, v87 row_ror:8 row_mask:0xf bank_mask:0x3
	v_mov_b32_dpp v84, v218 row_ror:8 row_mask:0xf bank_mask:0xc
	v_mov_b32_dpp v85, v219 row_ror:8 row_mask:0xf bank_mask:0xc
	v_mov_b32_dpp v86, v220 row_ror:8 row_mask:0xf bank_mask:0xc
	v_mov_b32_dpp v87, v221 row_ror:8 row_mask:0xf bank_mask:0xc
	v_lshl_add_u64 v[168:169], v[158:159], 0, s[52:53]
	global_store_dwordx4 v[158:159], v[84:87], off
; __device__ __forceinline__ unsigned cvt_pk_f16(float lo, float hi) { f32x2 v = {lo, hi}; h16x2 b = __builtin_convertvector(v, h16x2); return __builtin_bit_cast(unsigned, b); }
; #define PG8_BAR __builtin_amdgcn_s_barrier()
; #define PG8_BAR __builtin_amdgcn_s_barrier()
;     __device__ __forceinline__ void operator()(const f32x4 (&acc)[2][2][4][2], const Unit& u, int wr, int wc, int fr, int fq) const {
;         const int row0 = u.pm * BM + wr * 64 + fr, col0 = u.pn * BM + wc * 32 + 8 * fq;
; #pragma unroll
;         for (int ai = 0; ai < 2; ++ai)
; #pragma unroll
;             for (int m = 0; m < 4; ++m) { h16* rowp = C + (size_t)(row0 + ai * HALF + m * 16) * ldc + col0;
; #pragma unroll
;                 for (int bj = 0; bj < 2; ++bj) { const f32x4 v0 = acc[ai][bj][m][0], v1 = acc[ai][bj][m][1];
;                     u32x4 w; w.x = cvt_pk_f16(v0[0], v0[1]); w.y = cvt_pk_f16(v0[2], v0[3]); w.z = cvt_pk_f16(v1[0], v1[1]); w.w = cvt_pk_f16(v1[2], v1[3]);
;                     *(u32x4*)(rowp + bj * HALF) = w; } }
; template <class Epi, class Sched, bool ALIGN_EPI = true>
; __device__ __forceinline__ void gemm_phase(PG8_LAS unsigned char* lds, const Gemm g, const Sched& S, const Epi& E) {
;     ...
;         if constexpr (ALIGN_EPI) { if (wr == 0) PG8_BAR; }
;         if constexpr (!Epi::AFTER_DRAIN) E(acc, cur, wr, wc, fr, fq);
;         if (!has_next) break;
; #pragma unroll
;         for (int a = 0; a < 2; ++a)
; #pragma unroll
;             for (int b = 0; b < 2; ++b)
; #pragma unroll
;                 for (int m = 0; m < 4; ++m)
; #pragma unroll
;                     for (int n = 0; n < 2; ++n) acc[a][b][m][n] = (f32x4){0.f, 0.f, 0.f, 0.f};
;         cur = nxt; cA = nA; cB = nB; ++ui;
;         if constexpr (ALIGN_EPI) { if (wr == 1) PG8_BAR; }
	global_store_dwordx4 v[168:169], v[68:71], off
	v_cvt_pk_f16_f32 v60, v60, v61
	v_cvt_pk_f16_f32 v61, v62, v63
	v_cvt_pk_f16_f32 v62, v56, v57
	v_cvt_pk_f16_f32 v63, v58, v59
	v_cvt_pk_f16_f32 v44, v44, v45
	v_cvt_pk_f16_f32 v45, v46, v47
	v_cvt_pk_f16_f32 v46, v40, v41
	v_cvt_pk_f16_f32 v47, v42, v43
	v_mov_b32_e32 v218, v44
	v_mov_b32_e32 v219, v45
	v_mov_b32_e32 v220, v46
	v_mov_b32_e32 v221, v47
	s_nop 1
	v_mov_b32_dpp v44, v60 row_ror:8 row_mask:0xf bank_mask:0x3
	v_mov_b32_dpp v45, v61 row_ror:8 row_mask:0xf bank_mask:0x3
	v_mov_b32_dpp v46, v62 row_ror:8 row_mask:0xf bank_mask:0x3
	v_mov_b32_dpp v47, v63 row_ror:8 row_mask:0xf bank_mask:0x3
	v_mov_b32_dpp v60, v218 row_ror:8 row_mask:0xf bank_mask:0xc
	v_mov_b32_dpp v61, v219 row_ror:8 row_mask:0xf bank_mask:0xc
	v_mov_b32_dpp v62, v220 row_ror:8 row_mask:0xf bank_mask:0xc
	v_mov_b32_dpp v63, v221 row_ror:8 row_mask:0xf bank_mask:0xc
	v_lshl_add_u64 v[168:169], v[160:161], 0, s[52:53]
	global_store_dwordx4 v[160:161], v[60:63], off
	global_store_dwordx4 v[168:169], v[44:47], off
	v_cvt_pk_f16_f32 v52, v52, v53
	v_cvt_pk_f16_f32 v53, v54, v55
	v_cvt_pk_f16_f32 v54, v48, v49
	v_cvt_pk_f16_f32 v55, v50, v51
	v_cvt_pk_f16_f32 v28, v28, v29
	v_cvt_pk_f16_f32 v29, v30, v31
	v_cvt_pk_f16_f32 v30, v24, v25
	v_cvt_pk_f16_f32 v31, v26, v27
	v_mov_b32_e32 v218, v28
	v_mov_b32_e32 v219, v29
	v_mov_b32_e32 v220, v30
	v_mov_b32_e32 v221, v31
	s_nop 1
	v_mov_b32_dpp v28, v52 row_ror:8 row_mask:0xf bank_mask:0x3
	v_mov_b32_dpp v29, v53 row_ror:8 row_mask:0xf bank_mask:0x3
	v_mov_b32_dpp v30, v54 row_ror:8 row_mask:0xf bank_mask:0x3
	v_mov_b32_dpp v31, v55 row_ror:8 row_mask:0xf bank_mask:0x3
	v_mov_b32_dpp v52, v218 row_ror:8 row_mask:0xf bank_mask:0xc
	v_mov_b32_dpp v53, v219 row_ror:8 row_mask:0xf bank_mask:0xc
	v_mov_b32_dpp v54, v220 row_ror:8 row_mask:0xf bank_mask:0xc
	v_mov_b32_dpp v55, v221 row_ror:8 row_mask:0xf bank_mask:0xc
	v_lshl_add_u64 v[168:169], v[162:163], 0, s[52:53]
	global_store_dwordx4 v[162:163], v[52:55], off
	global_store_dwordx4 v[168:169], v[28:31], off
	v_cvt_pk_f16_f32 v36, v36, v37
	v_cvt_pk_f16_f32 v37, v38, v39
	v_cvt_pk_f16_f32 v38, v32, v33
	v_cvt_pk_f16_f32 v39, v34, v35
	v_cvt_pk_f16_f32 v12, v12, v13
	v_cvt_pk_f16_f32 v13, v14, v15
	v_cvt_pk_f16_f32 v14, v8, v9
	v_cvt_pk_f16_f32 v15, v10, v11
	v_mov_b32_e32 v218, v12
	v_mov_b32_e32 v219, v13
	v_mov_b32_e32 v220, v14
	v_mov_b32_e32 v221, v15
	s_nop 1
	v_mov_b32_dpp v12, v36 row_ror:8 row_mask:0xf bank_mask:0x3
	v_mov_b32_dpp v13, v37 row_ror:8 row_mask:0xf bank_mask:0x3
	v_mov_b32_dpp v14, v38 row_ror:8 row_mask:0xf bank_mask:0x3
	v_mov_b32_dpp v15, v39 row_ror:8 row_mask:0xf bank_mask:0x3
	v_mov_b32_dpp v36, v218 row_ror:8 row_mask:0xf bank_mask:0xc
	v_mov_b32_dpp v37, v219 row_ror:8 row_mask:0xf bank_mask:0xc
	v_mov_b32_dpp v38, v220 row_ror:8 row_mask:0xf bank_mask:0xc
	v_mov_b32_dpp v39, v221 row_ror:8 row_mask:0xf bank_mask:0xc
	v_lshl_add_u64 v[168:169], v[164:165], 0, s[52:53]
	global_store_dwordx4 v[164:165], v[36:39], off
	global_store_dwordx4 v[168:169], v[12:15], off
	v_cvt_pk_f16_f32 v20, v20, v21
	v_cvt_pk_f16_f32 v21, v22, v23
	v_cvt_pk_f16_f32 v22, v16, v17
	v_cvt_pk_f16_f32 v23, v18, v19
	v_cvt_pk_f16_f32 v4, v4, v5
	v_cvt_pk_f16_f32 v5, v6, v7
	v_cvt_pk_f16_f32 v6, v0, v1
	v_cvt_pk_f16_f32 v7, v2, v3
	v_mov_b32_e32 v218, v4
	v_mov_b32_e32 v219, v5
	v_mov_b32_e32 v220, v6
	v_mov_b32_e32 v221, v7
	s_nop 1
	v_mov_b32_dpp v4, v20 row_ror:8 row_mask:0xf bank_mask:0x3
	v_mov_b32_dpp v5, v21 row_ror:8 row_mask:0xf bank_mask:0x3
	v_mov_b32_dpp v6, v22 row_ror:8 row_mask:0xf bank_mask:0x3
	v_mov_b32_dpp v7, v23 row_ror:8 row_mask:0xf bank_mask:0x3
	v_mov_b32_dpp v20, v218 row_ror:8 row_mask:0xf bank_mask:0xc
	v_mov_b32_dpp v21, v219 row_ror:8 row_mask:0xf bank_mask:0xc
	v_mov_b32_dpp v22, v220 row_ror:8 row_mask:0xf bank_mask:0xc
	v_mov_b32_dpp v23, v221 row_ror:8 row_mask:0xf bank_mask:0xc
	v_lshl_add_u64 v[168:169], v[166:167], 0, s[52:53]
	global_store_dwordx4 v[166:167], v[20:23], off
	global_store_dwordx4 v[168:169], v[4:7], off
.Lproj_epi_join:
	s_andn2_b64 vcc, exec, s[38:39]
	s_mov_b64 s[38:39], -1
	s_mov_b32 s44, 0x800000
	s_cbranch_vccnz .LBB0_976
	s_andn2_b64 vcc, exec, s[0:1]
	s_cbranch_vccnz .LBB0_975
	s_barrier
	s_branch .LBB0_975
; __device__ __forceinline__ unsigned cvt_pk_f16(float lo, float hi) { f32x2 v = {lo, hi}; h16x2 b = __builtin_convertvector(v, h16x2); return __builtin_bit_cast(unsigned, b); }
;     __device__ __forceinline__ void operator()(const f32x4 (&acc)[2][2][4][2], const Unit& u, int wr, int wc, int fr, int fq) const {
;         const int row0 = u.pm * BM + wr * 64 + fr, col0 = u.pn * BM + wc * 32 + 8 * fq;
; #pragma unroll
;         for (int ai = 0; ai < 2; ++ai)
; #pragma unroll
;             for (int m = 0; m < 4; ++m) { h16* rowp = C + (size_t)(row0 + ai * HALF + m * 16) * ldc + col0;
; #pragma unroll
;                 for (int bj = 0; bj < 2; ++bj) { const f32x4 v0 = acc[ai][bj][m][0], v1 = acc[ai][bj][m][1];
;                     u32x4 w; w.x = cvt_pk_f16(v0[0], v0[1]); w.y = cvt_pk_f16(v0[2], v0[3]); w.z = cvt_pk_f16(v1[0], v1[1]); w.w = cvt_pk_f16(v1[2], v1[3]);
;                     *(u32x4*)(rowp + bj * HALF) = w; } }
.Lproj_epi_last:
	v_and_b32_e32 v224, -9, v140
	v_and_b32_e32 v225, 8, v140
	v_and_b32_e32 v226, 0x60, v142
	v_lshlrev_b32_e32 v225, 2, v225
	v_add3_u32 v226, v142, v226, v225
	v_lshl_add_u32 v150, s35, 8, v224
	v_lshl_or_b32 v144, s34, 8, v226
	v_ashrrev_i32_e32 v145, 31, v144
	v_mov_b64_e32 v[146:147], s[16:17]
	v_lshlrev_b64 v[144:145], 1, v[144:145]
	s_mov_b64 s[52:53], 0x1c000
	v_mad_i64_i32 v[152:153], s[34:35], v150, s91, v[146:147]
	v_lshl_add_u64 v[152:153], v[152:153], 0, v[144:145]
	v_add_u32_e32 v151, 0x10, v150
	v_mad_i64_i32 v[154:155], s[34:35], v151, s91, v[146:147]
	v_lshl_add_u64 v[154:155], v[154:155], 0, v[144:145]
	v_add_u32_e32 v151, 0x20, v150
	v_mad_i64_i32 v[156:157], s[34:35], v151, s91, v[146:147]
	v_lshl_add_u64 v[156:157], v[156:157], 0, v[144:145]
	v_add_u32_e32 v151, 0x30, v150
	v_mad_i64_i32 v[158:159], s[34:35], v151, s91, v[146:147]
	v_lshl_add_u64 v[158:159], v[158:159], 0, v[144:145]
	v_add_u32_e32 v151, 0x80, v150
	v_mad_i64_i32 v[160:161], s[34:35], v151, s91, v[146:147]
	v_lshl_add_u64 v[160:161], v[160:161], 0, v[144:145]
	v_add_u32_e32 v151, 0x90, v150
	v_mad_i64_i32 v[162:163], s[34:35], v151, s91, v[146:147]
	v_lshl_add_u64 v[162:163], v[162:163], 0, v[144:145]
	v_add_u32_e32 v151, 0xa0, v150
	v_mad_i64_i32 v[164:165], s[34:35], v151, s91, v[146:147]
	v_lshl_add_u64 v[164:165], v[164:165], 0, v[144:145]
	v_add_u32_e32 v151, 0xb0, v150
	v_mad_i64_i32 v[166:167], s[34:35], v151, s91, v[146:147]
	v_lshl_add_u64 v[166:167], v[166:167], 0, v[144:145]
	v_cvt_pk_f16_f32 v126, v126, v127
	v_cvt_pk_f16_f32 v127, v128, v129
	v_cvt_pk_f16_f32 v128, v122, v123
	v_cvt_pk_f16_f32 v129, v124, v125
	v_cvt_pk_f16_f32 v110, v110, v111
	v_cvt_pk_f16_f32 v111, v112, v113
	v_cvt_pk_f16_f32 v112, v106, v107
	v_cvt_pk_f16_f32 v113, v108, v109
	v_mov_b32_e32 v218, v110
	v_mov_b32_e32 v219, v111
	v_mov_b32_e32 v220, v112
	v_mov_b32_e32 v221, v113
	s_nop 1
	v_mov_b32_dpp v110, v126 row_ror:8 row_mask:0xf bank_mask:0x3
	v_mov_b32_dpp v111, v127 row_ror:8 row_mask:0xf bank_mask:0x3
	v_mov_b32_dpp v112, v128 row_ror:8 row_mask:0xf bank_mask:0x3
	v_mov_b32_dpp v113, v129 row_ror:8 row_mask:0xf bank_mask:0x3
	v_mov_b32_dpp v126, v218 row_ror:8 row_mask:0xf bank_mask:0xc
	v_mov_b32_dpp v127, v219 row_ror:8 row_mask:0xf bank_mask:0xc
	v_mov_b32_dpp v128, v220 row_ror:8 row_mask:0xf bank_mask:0xc
	v_mov_b32_dpp v129, v221 row_ror:8 row_mask:0xf bank_mask:0xc
	v_lshl_add_u64 v[168:169], v[152:153], 0, s[52:53]
	global_store_dwordx4 v[152:153], v[126:129], off sc1
	global_store_dwordx4 v[168:169], v[110:113], off sc1
	v_cvt_pk_f16_f32 v118, v118, v119
	v_cvt_pk_f16_f32 v119, v120, v121
	v_cvt_pk_f16_f32 v120, v114, v115
	v_cvt_pk_f16_f32 v121, v116, v117
	v_cvt_pk_f16_f32 v92, v92, v93
	v_cvt_pk_f16_f32 v93, v94, v95
	v_cvt_pk_f16_f32 v94, v88, v89
	v_cvt_pk_f16_f32 v95, v90, v91
	v_mov_b32_e32 v218, v92
	v_mov_b32_e32 v219, v93
	v_mov_b32_e32 v220, v94
	v_mov_b32_e32 v221, v95
	s_nop 1
	v_mov_b32_dpp v92, v118 row_ror:8 row_mask:0xf bank_mask:0x3
	v_mov_b32_dpp v93, v119 row_ror:8 row_mask:0xf bank_mask:0x3
	v_mov_b32_dpp v94, v120 row_ror:8 row_mask:0xf bank_mask:0x3
	v_mov_b32_dpp v95, v121 row_ror:8 row_mask:0xf bank_mask:0x3
	v_mov_b32_dpp v118, v218 row_ror:8 row_mask:0xf bank_mask:0xc
	v_mov_b32_dpp v119, v219 row_ror:8 row_mask:0xf bank_mask:0xc
	v_mov_b32_dpp v120, v220 row_ror:8 row_mask:0xf bank_mask:0xc
	v_mov_b32_dpp v121, v221 row_ror:8 row_mask:0xf bank_mask:0xc
	v_lshl_add_u64 v[168:169], v[154:155], 0, s[52:53]
	global_store_dwordx4 v[154:155], v[118:121], off sc1
	global_store_dwordx4 v[168:169], v[92:95], off sc1
	v_cvt_pk_f16_f32 v102, v102, v103
	v_cvt_pk_f16_f32 v103, v104, v105
	v_cvt_pk_f16_f32 v104, v98, v99
	v_cvt_pk_f16_f32 v105, v100, v101
	v_cvt_pk_f16_f32 v76, v76, v77
	v_cvt_pk_f16_f32 v77, v78, v79
	v_cvt_pk_f16_f32 v78, v72, v73
	v_cvt_pk_f16_f32 v79, v74, v75
	v_mov_b32_e32 v218, v76
	v_mov_b32_e32 v219, v77
	v_mov_b32_e32 v220, v78
	v_mov_b32_e32 v221, v79
	s_nop 1
	v_mov_b32_dpp v76, v102 row_ror:8 row_mask:0xf bank_mask:0x3
	v_mov_b32_dpp v77, v103 row_ror:8 row_mask:0xf bank_mask:0x3
	v_mov_b32_dpp v78, v104 row_ror:8 row_mask:0xf bank_mask:0x3
	v_mov_b32_dpp v79, v105 row_ror:8 row_mask:0xf bank_mask:0x3
	v_mov_b32_dpp v102, v218 row_ror:8 row_mask:0xf bank_mask:0xc
	v_mov_b32_dpp v103, v219 row_ror:8 row_mask:0xf bank_mask:0xc
	v_mov_b32_dpp v104, v220 row_ror:8 row_mask:0xf bank_mask:0xc
	v_mov_b32_dpp v105, v221 row_ror:8 row_mask:0xf bank_mask:0xc
	v_lshl_add_u64 v[168:169], v[156:157], 0, s[52:53]
	global_store_dwordx4 v[156:157], v[102:105], off sc1
	global_store_dwordx4 v[168:169], v[76:79], off sc1
	v_cvt_pk_f16_f32 v84, v84, v85
	v_cvt_pk_f16_f32 v85, v86, v87
	v_cvt_pk_f16_f32 v86, v80, v81
	v_cvt_pk_f16_f32 v87, v82, v83
	v_cvt_pk_f16_f32 v68, v68, v69
	v_cvt_pk_f16_f32 v69, v70, v71
	v_cvt_pk_f16_f32 v70, v64, v65
; __device__ __forceinline__ unsigned cvt_pk_f16(float lo, float hi) { f32x2 v = {lo, hi}; h16x2 b = __builtin_convertvector(v, h16x2); return __builtin_bit_cast(unsigned, b); }
;     __device__ __forceinline__ void operator()(const f32x4 (&acc)[2][2][4][2], const Unit& u, int wr, int wc, int fr, int fq) const {
;         const int row0 = u.pm * BM + wr * 64 + fr, col0 = u.pn * BM + wc * 32 + 8 * fq;
; #pragma unroll
;         for (int ai = 0; ai < 2; ++ai)
; #pragma unroll
;             for (int m = 0; m < 4; ++m) { h16* rowp = C + (size_t)(row0 + ai * HALF + m * 16) * ldc + col0;
; #pragma unroll
;                 for (int bj = 0; bj < 2; ++bj) { const f32x4 v0 = acc[ai][bj][m][0], v1 = acc[ai][bj][m][1];
;                     u32x4 w; w.x = cvt_pk_f16(v0[0], v0[1]); w.y = cvt_pk_f16(v0[2], v0[3]); w.z = cvt_pk_f16(v1[0], v1[1]); w.w = cvt_pk_f16(v1[2], v1[3]);
;                     *(u32x4*)(rowp + bj * HALF) = w; } }
	v_cvt_pk_f16_f32 v71, v66, v67
	v_mov_b32_e32 v218, v68
	v_mov_b32_e32 v219, v69
	v_mov_b32_e32 v220, v70
	v_mov_b32_e32 v221, v71
	s_nop 1
	v_mov_b32_dpp v68, v84 row_ror:8 row_mask:0xf bank_mask:0x3
	v_mov_b32_dpp v69, v85 row_ror:8 row_mask:0xf bank_mask:0x3
	v_mov_b32_dpp v70, v86 row_ror:8 row_mask:0xf bank_mask:0x3
	v_mov_b32_dpp v71, v87 row_ror:8 row_mask:0xf bank_mask:0x3
	v_mov_b32_dpp v84, v218 row_ror:8 row_mask:0xf bank_mask:0xc
	v_mov_b32_dpp v85, v219 row_ror:8 row_mask:0xf bank_mask:0xc
	v_mov_b32_dpp v86, v220 row_ror:8 row_mask:0xf bank_mask:0xc
	v_mov_b32_dpp v87, v221 row_ror:8 row_mask:0xf bank_mask:0xc
	v_lshl_add_u64 v[168:169], v[158:159], 0, s[52:53]
	global_store_dwordx4 v[158:159], v[84:87], off sc1
	global_store_dwordx4 v[168:169], v[68:71], off sc1
	v_cvt_pk_f16_f32 v60, v60, v61
	v_cvt_pk_f16_f32 v61, v62, v63
	v_cvt_pk_f16_f32 v62, v56, v57
	v_cvt_pk_f16_f32 v63, v58, v59
	v_cvt_pk_f16_f32 v44, v44, v45
	v_cvt_pk_f16_f32 v45, v46, v47
	v_cvt_pk_f16_f32 v46, v40, v41
	v_cvt_pk_f16_f32 v47, v42, v43
	v_mov_b32_e32 v218, v44
	v_mov_b32_e32 v219, v45
	v_mov_b32_e32 v220, v46
	v_mov_b32_e32 v221, v47
	s_nop 1
	v_mov_b32_dpp v44, v60 row_ror:8 row_mask:0xf bank_mask:0x3
	v_mov_b32_dpp v45, v61 row_ror:8 row_mask:0xf bank_mask:0x3
	v_mov_b32_dpp v46, v62 row_ror:8 row_mask:0xf bank_mask:0x3
	v_mov_b32_dpp v47, v63 row_ror:8 row_mask:0xf bank_mask:0x3
	v_mov_b32_dpp v60, v218 row_ror:8 row_mask:0xf bank_mask:0xc
	v_mov_b32_dpp v61, v219 row_ror:8 row_mask:0xf bank_mask:0xc
	v_mov_b32_dpp v62, v220 row_ror:8 row_mask:0xf bank_mask:0xc
	v_mov_b32_dpp v63, v221 row_ror:8 row_mask:0xf bank_mask:0xc
	v_lshl_add_u64 v[168:169], v[160:161], 0, s[52:53]
	global_store_dwordx4 v[160:161], v[60:63], off sc1
	global_store_dwordx4 v[168:169], v[44:47], off sc1
	v_cvt_pk_f16_f32 v52, v52, v53
	v_cvt_pk_f16_f32 v53, v54, v55
	v_cvt_pk_f16_f32 v54, v48, v49
	v_cvt_pk_f16_f32 v55, v50, v51
	v_cvt_pk_f16_f32 v28, v28, v29
	v_cvt_pk_f16_f32 v29, v30, v31
	v_cvt_pk_f16_f32 v30, v24, v25
	v_cvt_pk_f16_f32 v31, v26, v27
	v_mov_b32_e32 v218, v28
	v_mov_b32_e32 v219, v29
	v_mov_b32_e32 v220, v30
	v_mov_b32_e32 v221, v31
	s_nop 1
	v_mov_b32_dpp v28, v52 row_ror:8 row_mask:0xf bank_mask:0x3
	v_mov_b32_dpp v29, v53 row_ror:8 row_mask:0xf bank_mask:0x3
	v_mov_b32_dpp v30, v54 row_ror:8 row_mask:0xf bank_mask:0x3
	v_mov_b32_dpp v31, v55 row_ror:8 row_mask:0xf bank_mask:0x3
	v_mov_b32_dpp v52, v218 row_ror:8 row_mask:0xf bank_mask:0xc
	v_mov_b32_dpp v53, v219 row_ror:8 row_mask:0xf bank_mask:0xc
	v_mov_b32_dpp v54, v220 row_ror:8 row_mask:0xf bank_mask:0xc
	v_mov_b32_dpp v55, v221 row_ror:8 row_mask:0xf bank_mask:0xc
	v_lshl_add_u64 v[168:169], v[162:163], 0, s[52:53]
	global_store_dwordx4 v[162:163], v[52:55], off sc1
	global_store_dwordx4 v[168:169], v[28:31], off sc1
	v_cvt_pk_f16_f32 v36, v36, v37
	v_cvt_pk_f16_f32 v37, v38, v39
	v_cvt_pk_f16_f32 v38, v32, v33
	v_cvt_pk_f16_f32 v39, v34, v35
	v_cvt_pk_f16_f32 v12, v12, v13
	v_cvt_pk_f16_f32 v13, v14, v15
	v_cvt_pk_f16_f32 v14, v8, v9
	v_cvt_pk_f16_f32 v15, v10, v11
	v_mov_b32_e32 v218, v12
	v_mov_b32_e32 v219, v13
	v_mov_b32_e32 v220, v14
	v_mov_b32_e32 v221, v15
	s_nop 1
	v_mov_b32_dpp v12, v36 row_ror:8 row_mask:0xf bank_mask:0x3
	v_mov_b32_dpp v13, v37 row_ror:8 row_mask:0xf bank_mask:0x3
	v_mov_b32_dpp v14, v38 row_ror:8 row_mask:0xf bank_mask:0x3
	v_mov_b32_dpp v15, v39 row_ror:8 row_mask:0xf bank_mask:0x3
	v_mov_b32_dpp v36, v218 row_ror:8 row_mask:0xf bank_mask:0xc
	v_mov_b32_dpp v37, v219 row_ror:8 row_mask:0xf bank_mask:0xc
	v_mov_b32_dpp v38, v220 row_ror:8 row_mask:0xf bank_mask:0xc
	v_mov_b32_dpp v39, v221 row_ror:8 row_mask:0xf bank_mask:0xc
	v_lshl_add_u64 v[168:169], v[164:165], 0, s[52:53]
	global_store_dwordx4 v[164:165], v[36:39], off sc1
	global_store_dwordx4 v[168:169], v[12:15], off sc1
	v_cvt_pk_f16_f32 v20, v20, v21
	v_cvt_pk_f16_f32 v21, v22, v23
	v_cvt_pk_f16_f32 v22, v16, v17
	v_cvt_pk_f16_f32 v23, v18, v19
	v_cvt_pk_f16_f32 v4, v4, v5
	v_cvt_pk_f16_f32 v5, v6, v7
	v_cvt_pk_f16_f32 v6, v0, v1
	v_cvt_pk_f16_f32 v7, v2, v3
	v_mov_b32_e32 v218, v4
	v_mov_b32_e32 v219, v5
	v_mov_b32_e32 v220, v6
	v_mov_b32_e32 v221, v7
	s_nop 1
	v_mov_b32_dpp v4, v20 row_ror:8 row_mask:0xf bank_mask:0x3
	v_mov_b32_dpp v5, v21 row_ror:8 row_mask:0xf bank_mask:0x3
	v_mov_b32_dpp v6, v22 row_ror:8 row_mask:0xf bank_mask:0x3
	v_mov_b32_dpp v7, v23 row_ror:8 row_mask:0xf bank_mask:0x3
	v_mov_b32_dpp v20, v218 row_ror:8 row_mask:0xf bank_mask:0xc
	v_mov_b32_dpp v21, v219 row_ror:8 row_mask:0xf bank_mask:0xc
	v_mov_b32_dpp v22, v220 row_ror:8 row_mask:0xf bank_mask:0xc
	v_mov_b32_dpp v23, v221 row_ror:8 row_mask:0xf bank_mask:0xc
	v_lshl_add_u64 v[168:169], v[166:167], 0, s[52:53]
	global_store_dwordx4 v[166:167], v[20:23], off sc1
	global_store_dwordx4 v[168:169], v[4:7], off sc1
	s_branch .Lproj_epi_join
